# unused
# baseline (speedup 1.0000x reference)
; __device__ __forceinline__ int tid_fresh() { int t = threadIdx.x; asm volatile("" : "+v"(t)); return t; }
; #define PG8_STAGE(bufoff, gbase, v0, v1) do { \
;         __builtin_amdgcn_global_load_lds((const unsigned*)((const char*)(gbase) + (v0)), (LAS unsigned*)(lds + (bufoff) + ldsw), 16, 0, 0); \
;         __builtin_amdgcn_global_load_lds((const unsigned*)((const char*)(gbase) + (v1)), (LAS unsigned*)(lds + (bufoff) + ldsw + 8192), 16, 0, 0); } while (0)
; #define PG8_BAR __builtin_amdgcn_s_barrier()
; template <class Epi, class Sched>
; __device__ __forceinline__ void gemm_phase(LAS unsigned char* lds, const int K, const Sched& S, const Epi& E) {
;     const int tid = tid_fresh(), wid = __builtin_amdgcn_readfirstlane(tid >> 6), lane = tid & 63, wr = wid >> 2, wc = wid & 3, fr = lane & 15, fq = lane >> 4;
;     const int nt = K / BK;
;     int R0, C0, R1, C1; stage_rc(tid * 16, R0, C0); stage_rc(tid * 16 + 8192, R1, C1);
;     const int Rb0 = Epi::PERM ? ((R0 & ~31) + perm32(R0 & 31)) : R0, Rb1 = Epi::PERM ? ((R1 & ~31) + perm32(R1 & 31)) : R1;
;     const unsigned voffB0 = S.b_off(Rb0, C0), voffB1 = S.b_off(Rb1, C1);
;     const size_t kstep = (size_t)(BK * 2);
;     const size_t kstepB = S.b_kstep(), hstep = S.b_hstep();
;     const unsigned ldsw = (unsigned)wid * 1024u;
;     const int aoff = lds_byte(wr * 64 + fr, fq * 8), boff = lds_byte(wc * 32 + fr, fq * 8);
;     ...
;     Unit cur, nxt; int ui = 0;
;     if (!S.next(0, cur)) return;
;     f32x4 acc[2][2][4][2];
; #pragma unroll
;     for (int a = 0; a < 2; ++a)
; #pragma unroll
;         for (int b = 0; b < 2; ++b)
; #pragma unroll
;             for (int m = 0; m < 4; ++m)
; #pragma unroll
;                 for (int n = 0; n < 2; ++n) acc[a][b][m][n] = (f32x4){0.f, 0.f, 0.f, 0.f};
;     bf16x8 At[4][2], B0[2][2], B1[2][2];
;     const char* const gA = S.a_base();
;     unsigned c00, c01, c10, c11, n00, n01, n10, n11;
;     PG8_AOFFS(cur, c00, c01, c10, c11);
;     const char* cB = S.b_ptr(cur);
;     PG8_STAGE(PG8_SB(0, 0), cB, voffB0, voffB1); PG8_STAGE(PG8_SA(0, 0), gA, c00, c01); PG8_STAGE(PG8_SB(0, 1), cB + hstep, voffB0, voffB1); PG8_STAGE(PG8_SA(0, 1), gA, c10, c11);
;     if (wr == 1) PG8_BAR;
;     PG8_WAIT_V(4); PG8_BAR;
;     PG8_STAGE(PG8_SB(1, 0), cB + kstepB, voffB0, voffB1); PG8_STAGE(PG8_SA(1, 0), gA + kstep, c00, c01); PG8_STAGE(PG8_SB(1, 1), cB + hstep + kstepB, voffB0, voffB1);
.LBB0_1152:
	s_or_b64 exec, exec, s[0:1]
	v_readlane_b32 s0, v254, 0
	v_readlane_b32 s2, v254, 5
	v_readlane_b32 s1, v254, 1
	s_lshl_b32 s15, s28, 3
	s_and_b32 s3, s2, 7
	v_mov_b32_e32 v2, v0
	s_waitcnt lgkmcnt(0)
	s_barrier
	v_readlane_b32 s84, v254, 0
	v_readlane_b32 s85, v254, 1
	s_nop 1
	s_load_dwordx2 s[74:75], s[84:85], 0xd8
	s_load_dwordx2 s[76:77], s[84:85], 0xe0
	s_load_dwordx2 s[78:79], s[84:85], 0x118
	v_and_b32_e32 v252, 63, v0
	v_lshrrev_b32_e32 v253, 6, v0
	v_lshlrev_b32_e32 v238, 2, v252
	v_lshlrev_b32_e32 v252, 4, v252
	v_add_u32_e32 v239, 0x800, v238
	v_add_u32_e32 v240, 0x1000, v238
	v_add_u32_e32 v241, 0x1800, v238
	v_readlane_b32 s86, v254, 4
	v_readlane_b32 s87, v255, 40
	v_readfirstlane_b32 s88, v253
	s_nop 3
	s_lshl_b32 s71, s86, 3
	s_lshl_b32 s87, s87, 3
	s_add_u32 s87, s87, s88
	s_add_u32 s70, s87, 0x24000
	s_mov_b32 s80, 0
	s_mov_b32 s82, 0
	s_mov_b32 s90, 0
	s_waitcnt lgkmcnt(0)
	v_writelane_b32 v254, s3, 39
	s_cmp_lt_i32 s2, s15
	s_nop 0
	v_readfirstlane_b32 s33, v2
	s_cbranch_scc0 .LBB0_1166
	v_ashrrev_i32_e32 v1, 31, v2
	v_lshrrev_b32_e32 v1, 26, v1
	v_add_u32_e32 v1, v2, v1
	v_ashrrev_i32_e32 v4, 6, v1
	v_bfe_i32 v1, v2, 27, 1
	v_lshlrev_b32_e32 v3, 4, v2
	v_lshrrev_b32_e32 v1, 22, v1
	v_add_u32_e32 v1, v3, v1
	v_and_b32_e32 v1, 0xfffffc00, v1
	v_sub_u32_e32 v1, v3, v1
	v_lshrrev_b32_e32 v5, 4, v1
	v_bitop3_b32 v5, v5, v1, 32 bitop3:0x6c
	v_ashrrev_i32_e32 v1, 31, v1
	v_lshrrev_b32_e32 v1, 26, v1
	v_lshlrev_b32_e32 v6, 3, v4
	v_add_u32_e32 v1, v5, v1
	v_and_b32_e32 v6, -16, v6
	v_ashrrev_i32_e32 v7, 6, v1
	v_add_u32_e32 v3, 0x2000, v3
	v_add_u32_e32 v1, v7, v6
	v_ashrrev_i32_e32 v6, 31, v3
	v_lshrrev_b32_e32 v6, 22, v6
	v_add_u32_e32 v6, v3, v6
	s_load_dwordx2 s[0:1], s[0:1], 0x118
	v_ashrrev_i32_e32 v6, 10, v6
	v_mul_i32_i24_e32 v8, 0x400, v6
	v_sub_u32_e32 v3, v3, v8
	v_lshrrev_b32_e32 v8, 4, v3
	v_bitop3_b32 v3, v8, v3, 32 bitop3:0x6c
	s_waitcnt lgkmcnt(0)
	s_add_u32 s2, s0, 0x3ee90000
	v_ashrrev_i32_e32 v9, 31, v3
	s_addc_u32 s3, s1, 0
	v_lshrrev_b32_e32 v9, 26, v9
	s_add_u32 s46, s0, 0x24830000
	v_add_u32_e32 v9, v3, v9
	s_addc_u32 s47, s1, 0
	s_ashr_i32 s11, s33, 6
	v_lshlrev_b32_e32 v8, 3, v6
	v_ashrrev_i32_e32 v10, 6, v9
	v_readlane_b32 s4, v254, 39
	v_and_b32_e32 v9, 0xc0, v9
	s_ashr_i32 s10, s33, 8
	v_and_b32_e32 v8, -16, v8
	s_lshl_b32 s48, s11, 10
	s_lshl_b32 s4, s4, 12
	v_lshlrev_b32_e32 v6, 5, v6
	v_sub_u32_e32 v3, v3, v9
	v_mov_b32_e32 v9, 1
	v_add_u32_e32 v146, v10, v8
	s_add_u32 s8, s46, s4
	v_readlane_b32 s4, v254, 5
	v_and_b32_e32 v6, 32, v6
	v_ashrrev_i16_sdwa v3, v9, sext(v3) dst_sel:DWORD dst_unused:UNUSED_PAD src0_sel:DWORD src1_sel:BYTE_0
	s_addc_u32 s9, s47, 0
	s_ashr_i32 s12, s4, 3
	v_and_b32_e32 v8, 3, v10
	s_mov_b32 s5, 0xfffffe0
	v_lshlrev_b32_e32 v10, 1, v146
	v_lshrrev_b32_e32 v11, 2, v146
	v_add_u32_sdwa v3, v6, sext(v3) dst_sel:DWORD dst_unused:UNUSED_PAD src0_sel:DWORD src1_sel:WORD_0
	s_lshl_b32 s4, s12, 2
	v_and_or_b32 v8, v146, s5, v8
	v_and_b32_e32 v10, 24, v10
	v_and_b32_e32 v11, 4, v11
	v_lshlrev_b32_e32 v6, 8, v3
	s_add_i32 s4, s4, 0
	v_or3_b32 v8, v8, v10, v11
	v_and_b32_e32 v6, 0xffff800, v6
	s_add_i32 s4, s4, 0x21160
	v_add_lshl_u32 v130, v8, v6, 4
	v_and_b32_e32 v6, 3, v7
	v_mul_i32_i24_e32 v7, 64, v7
	v_sub_u32_e32 v5, v5, v7
	v_mov_b32_e32 v7, s4
	ds_read_b32 v7, v7
	v_lshlrev_b32_e32 v8, 1, v1
	v_lshrrev_b32_e32 v10, 2, v1
	v_and_or_b32 v6, v1, s5, v6
	v_and_b32_e32 v8, 24, v8
	v_and_b32_e32 v10, 4, v10
	v_or3_b32 v6, v6, v8, v10
	s_waitcnt lgkmcnt(0)
	v_lshlrev_b32_e32 v8, 2, v7
	v_add_u32_e32 v8, 0, v8
	v_add_u32_e32 v8, 0x21040, v8
	ds_read_b32 v8, v8
	s_lshl_b32 s13, s12, 8
	v_readfirstlane_b32 s4, v7
	s_ashr_i32 s5, s4, 31
	v_lshlrev_b32_e32 v4, 5, v4
	s_waitcnt lgkmcnt(0)
	v_readfirstlane_b32 s14, v8
	s_sub_i32 s12, s12, s14
	s_lshl_b32 s12, s12, 8
	v_cmp_lt_i64_e64 s[6:7], s[4:5], 64
	s_add_i32 s12, s12, 0xff00
	v_and_b32_e32 v4, 32, v4
	v_ashrrev_i16_sdwa v5, v9, sext(v5) dst_sel:DWORD dst_unused:UNUSED_PAD src0_sel:DWORD src1_sel:BYTE_0
	s_and_b64 s[6:7], s[6:7], exec
	v_add_u32_sdwa v4, v4, sext(v5) dst_sel:DWORD dst_unused:UNUSED_PAD src0_sel:DWORD src1_sel:WORD_0
	s_cselect_b32 s12, s13, s12
	s_lshl_b64 s[4:5], s[4:5], 21
	v_lshlrev_b32_e32 v5, 8, v4
	s_add_u32 s38, s8, s4
	v_and_b32_e32 v5, 0xffff800, v5
	s_addc_u32 s39, s9, s5
	s_add_i32 s49, s48, 0
	v_add_lshl_u32 v132, v6, v5, 4
	s_add_i32 m0, s49, 0x10000
	v_add_u32_e32 v5, s12, v1
	v_lshlrev_b32_e32 v149, 1, v4
	v_mov_b32_e32 v135, 0
	global_load_lds_dwordx4 v132, s[38:39]
	s_add_i32 m0, s49, 0x12000
	v_add_u32_e32 v6, s12, v146
	v_add_u32_e32 v147, 0x80, v1
	v_lshl_add_u32 v134, v5, 10, v149
	v_lshlrev_b32_e32 v150, 1, v3
	v_mov_b32_e32 v133, v135
	global_load_lds_dwordx4 v130, s[38:39]
	s_mov_b32 m0, s49
	s_add_i32 s50, s49, 0x2000
	v_add_u32_e32 v7, s12, v147
	v_lshl_add_u32 v136, v6, 10, v150
	v_lshl_add_u64 v[4:5], s[38:39], 0, v[132:133]
	v_mov_b32_e32 v131, v135
	global_load_lds_dwordx4 v134, s[2:3]
	s_mov_b32 m0, s50
	s_mov_b64 s[4:5], 0x800
	v_lshl_add_u32 v138, v7, 10, v149
	v_lshl_add_u64 v[6:7], s[38:39], 0, v[130:131]
	global_load_lds_dwordx4 v136, s[2:3]
	v_lshl_add_u64 v[4:5], v[4:5], 0, s[4:5]
	s_add_i32 m0, s49, 0x14000
	v_add_u32_e32 v148, 0x80, v146
	global_load_lds_dwordx4 v[4:5], off
	v_lshl_add_u64 v[4:5], v[6:7], 0, s[4:5]
	s_add_i32 m0, s49, 0x16000
	s_add_i32 s51, s49, 0x4000
	v_add_u32_e32 v8, s12, v148
	global_load_lds_dwordx4 v[4:5], off
	s_mov_b32 m0, s51
	s_add_i32 s52, s49, 0x6000
	v_lshl_add_u32 v140, v8, 10, v150
	global_load_lds_dwordx4 v138, s[2:3]
	s_mov_b32 m0, s52
	s_mov_b32 s53, 0
	global_load_lds_dwordx4 v140, s[2:3]
	s_mov_b32 s54, 0x10000
	s_cmp_lg_u32 s10, 1
	v_mov_b32_e32 v137, v135
	s_cbranch_scc1 .LBB0_1155
	s_barrier

; #define PG8_WAIT_V(n) asm volatile("s_waitcnt vmcnt(" #n ")" ::: "memory")
; #define PG8_WAIT_L(n) asm volatile("s_waitcnt lgkmcnt(" #n ")" ::: "memory")
; template <class Epi, class Sched>
; __device__ __forceinline__ void gemm_phase(LAS unsigned char* lds, const int K, const Sched& S, const Epi& E) {
;     ...
;             PG8_LDB(B0, 0, 0); PG8_SCHED; PG8_LDA(At, 0, 0); PG8_STAGE(PG8_SA(1, 1), a1, c10, c11);
;             PG8_WAIT_L(8); PG8_BAR; PG8_WAIT_L(0); PG8_MMA(0, 0, At, B0); PG8_BAR; PG8_SCHED;
;             PG8_LDB(B1, 0, 1); PG8_STAGE(PG8_SB(0, 0), b2, voffB0, voffB1);
;             PG8_BAR; PG8_WAIT_L(0); PG8_MMA(0, 1, At, B1); PG8_BAR;
;             PG8_LDA(At, 0, 1); PG8_STAGE(PG8_SA(0, 0), a2, x00, x01);
;             PG8_BAR; PG8_WAIT_L(0); PG8_MMA(1, 0, At, B0); PG8_BAR; PG8_SCHED;
;             PG8_STAGE(PG8_SB(0, 1), b2 + hstep, voffB0, voffB1);
;             PG8_WAIT_V(6); PG8_BAR; PG8_MMA(1, 1, At, B1); PG8_BAR;
;             PG8_LDB(B0, 1, 0); PG8_SCHED; PG8_LDA(At, 1, 0); PG8_STAGE(PG8_SA(0, 1), a2, x10, x11);
;             PG8_WAIT_L(8); PG8_BAR; PG8_WAIT_L(0); PG8_MMA(0, 0, At, B0); PG8_BAR; PG8_SCHED;
;             PG8_LDB(B1, 1, 1); PG8_STAGE(PG8_SB(1, 0), b3, voffB0, voffB1);
;             PG8_BAR; PG8_WAIT_L(0); PG8_MMA(0, 1, At, B1); PG8_BAR;
;             PG8_LDA(At, 1, 1); PG8_STAGE(PG8_SA(1, 0), a3, x00, x01);
;             PG8_BAR; PG8_WAIT_L(0); PG8_MMA(1, 0, At, B0); PG8_BAR; PG8_SCHED;
;             PG8_STAGE(PG8_SB(1, 1), b3 + hstep, voffB0, voffB1);
;             PG8_WAIT_V(6); PG8_BAR; PG8_MMA(1, 1, At, B1); PG8_BAR;
; __device__ __forceinline__ bool bg_decode(int st, int wg, int NW, int lane, KP kp, const float*& src, int& ldS, bf16_t*& dst, int& o2) {
;     const int g = st * NW + wg;
;     if (g >= BG_STEPS) { src = kp->in[27] + lane; ldS = 0; dst = nullptr; o2 = 0; return false; }
;     const int l = g / 98304, r = g - l * 98304;
;     unsigned char* ws = kp->ws;
;     if (r < 65536) {
;         const int e = r >> 10, kc = (r >> 2) & 255, kind = (r >> 1) & 1, cc = r & 1, n = cc * 256 + lane;
;         ldS = FF; o2 = 256 * 8;
;         src = kp->in[27 + kind] + ((size_t)(l * NE + e) * D + kc * 8) * FF + n;
;         const int drow = (n >> 7) * 256 + kind * 128 + (n & 127);
;         dst = (bf16_t*)(ws + WS_WGU) + l * WGU_L + (size_t)e * 1024 * D + ((size_t)kc * 1024 + drow) * 8;
.Lpb9_p4j:
	s_barrier
	s_setprio 1
	v_mfma_f32_16x16x32_bf16 v[54:57], v[216:219], v[180:183], v[54:57]
	v_mfma_f32_16x16x32_bf16 v[50:53], v[224:227], v[180:183], v[50:53]
	v_mfma_f32_16x16x32_bf16 v[38:41], v[216:219], v[188:191], v[38:41]
	v_mfma_f32_16x16x32_bf16 v[34:37], v[224:227], v[188:191], v[34:37]
	v_mfma_f32_16x16x32_bf16 v[22:25], v[216:219], v[196:199], v[22:25]
	v_mfma_f32_16x16x32_bf16 v[18:21], v[224:227], v[196:199], v[18:21]
	v_mfma_f32_16x16x32_bf16 v[6:9], v[216:219], v[208:211], v[6:9]
	v_mfma_f32_16x16x32_bf16 v[2:5], v[224:227], v[208:211], v[2:5]
	v_mfma_f32_16x16x32_bf16 v[54:57], v[220:223], v[184:187], v[54:57]
	v_mfma_f32_16x16x32_bf16 v[50:53], v[228:231], v[184:187], v[50:53]
	v_mfma_f32_16x16x32_bf16 v[38:41], v[220:223], v[192:195], v[38:41]
	v_mfma_f32_16x16x32_bf16 v[34:37], v[228:231], v[192:195], v[34:37]
	v_mfma_f32_16x16x32_bf16 v[22:25], v[220:223], v[200:203], v[22:25]
	v_mfma_f32_16x16x32_bf16 v[18:21], v[228:231], v[200:203], v[18:21]
	v_mfma_f32_16x16x32_bf16 v[6:9], v[220:223], v[212:215], v[6:9]
	v_mfma_f32_16x16x32_bf16 v[2:5], v[228:231], v[212:215], v[2:5]
	s_setprio 0
	s_add_i32 s67, 0, 0x18000
	v_add_u32_e32 v134, s67, v151
	s_barrier
	ds_read_b128 v[164:167], v134
	ds_read_b128 v[168:171], v134 offset:1024
	ds_read_b128 v[172:175], v134 offset:2048
	ds_read_b128 v[176:179], v134 offset:3072
	s_mov_b32 m0, s51
	ds_read_b128 v[180:183], v154 offset:32768
	ds_read_b128 v[184:187], v154 offset:33792
	ds_read_b128 v[188:191], v154 offset:34816
	ds_read_b128 v[192:195], v154 offset:35840
	ds_read_b128 v[196:199], v154 offset:36864
	ds_read_b128 v[200:203], v154 offset:37888
	ds_read_b128 v[208:211], v154 offset:38912
	ds_read_b128 v[212:215], v154 offset:39936
	v_cndmask_b32_e32 v134, v140, v160, vcc
	global_load_lds_dwordx4 v139, s[44:45]
	s_mov_b32 m0, s52
	s_nop 0
	global_load_lds_dwordx4 v134, s[44:45]
	s_cmp_ge_u32 s70, 0x28000
	s_cbranch_scc1 .Lpb9_p5n
	s_cmp_eq_u32 s80, 0
	s_cbranch_scc0 .Lpb9_adv2
	s_cmp_ge_u32 s70, 0x18000
	s_cselect_b32 s84, 0x18000, 0
	s_cselect_b32 s83, 0x10000000, 0
	s_mov_b32 s81, 0x4030000
	s_cselect_b32 s81, 0x14430000, s81
	s_sub_u32 s84, s70, s84
	s_lshr_b32 s85, s84, 2
	s_lshl_b32 s85, s85, 14
	s_and_b32 s86, s84, 1
	s_lshl_b32 s87, s86, 10
	s_add_u32 s87, s87, s85
	s_add_u32 s87, s87, s83
	s_bitcmp1_b32 s84, 1
	s_cselect_b64 s[72:73], s[76:77], s[74:75]
	s_add_u32 s72, s72, s87
	s_addc_u32 s73, s73, 0
	s_add_u32 s88, s72, 0x2000
	s_addc_u32 s89, s73, 0
	s_lshl_b32 s86, s86, 13
	s_add_u32 s85, s85, s86
	s_and_b32 s86, s84, 2
	s_lshl_b32 s86, s86, 10
	s_add_u32 s85, s85, s86
	s_add_u32 s85, s85, s81
	v_add_u32_e32 v253, s85, v252
	s_movk_i32 s81, 0x400
	s_branch .Lpb9_ld2
